# v58 + one static s_setprio 1 at kernel entry for waves 4-7 (second-dispatched half of each SIMD pair)
# baseline (speedup 1.0000x reference)
; #define LAS __attribute__((address_space(3)))
; __global__ void __launch_bounds__(NTHR, 2) hybrid_fwd(Params P) {
;     ...
;     Ctx c; c.lds = (LAS unsigned char*)lds_raw; c.ws = P.ws; c.ctl = (unsigned*)(P.ws + WS_CTL);
;     c.wid = __builtin_amdgcn_readfirstlane(threadIdx.x >> 6); c.bid = blockIdx.x; c.G = gridDim.x;
;     volatile LAS unsigned* xbw = (volatile LAS unsigned*)(c.lds + LDS_BYTES - 16);
;     if (threadIdx.x == 0) { xbw[0] = 0u; xbw[1] = 0u; xbw[2] = 0u; xbw[3] = 0u; }
;     __syncthreads();
;     const XcdBarrier bar = xcd_barrier_post(c.ctl, xbw);
_ZN12_GLOBAL__N_110hybrid_fwdENS_6ParamsE:
	s_load_dwordx2 s[34:35], s[0:1], 0xe0
	s_load_dword s44, s[0:1], 0xe8
	s_add_u32 s92, s0, 0xe8
	s_mov_b32 s90, s2
	v_readfirstlane_b32 s88, v0
	s_addc_u32 s93, s1, 0
	s_cmp_lt_u32 s88, 0x100
	s_cbranch_scc1 .Lprio_done
	s_setprio 1
.Lprio_done:
	v_cmp_eq_u32_e64 s[2:3], 0, v0
	s_mov_b64 s[6:7], exec
	s_nop 0
	v_writelane_b32 v242, s2, 0
	s_nop 1
	v_writelane_b32 v242, s3, 1
	s_and_b64 s[2:3], s[6:7], s[2:3]
	s_mov_b64 exec, s[2:3]
	s_cbranch_execz .LBB0_2
	s_add_i32 s2, 0, 0x23ff0
	v_mov_b32_e32 v0, 0
	v_mov_b32_e32 v1, s2
	s_add_i32 s2, 0, 0x23ff4
	ds_write_b32 v1, v0
	v_mov_b32_e32 v1, s2
	s_add_i32 s2, 0, 0x23ff8
	ds_write_b32 v1, v0
	v_mov_b32_e32 v1, s2
	s_add_i32 s2, 0, 0x23ffc
	ds_write_b32 v1, v0
	v_mov_b32_e32 v1, s2
	ds_write_b32 v1, v0
